# stack: MoE block order 1,3,2,4 + A-tile DMA addresses precomputed for the back edge + P3c gate loads hoisted above stores + relaxed store drains
# speedup vs baseline: 1.0087x; 1.0087x over previous
.LBB0_732:
	s_cmp_lg_u64 s[2:3], 0
	s_cbranch_scc1 .Lswp_guO_half
	ds_read_b64_tr_b16 v[162:163], v190 offset:32768
	ds_read_b64_tr_b16 v[164:165], v191 offset:32768
	ds_read_b64_tr_b16 v[170:171], v192 offset:32768
	ds_read_b64_tr_b16 v[172:173], v193 offset:32768
	ds_read_b128 v[214:217], v207 offset:32768
	ds_read_b128 v[224:227], v207 offset:34816
	ds_read_b128 v[232:235], v207 offset:36864
	ds_read_b128 v[240:243], v207 offset:38912
	ds_read_b64_tr_b16 v[166:167], v190 offset:40960
	ds_read_b64_tr_b16 v[168:169], v191 offset:40960
	ds_read_b64_tr_b16 v[174:175], v192 offset:40960
	ds_read_b64_tr_b16 v[176:177], v193 offset:40960
	ds_read_b128 v[218:221], v207 offset:33792
	ds_read_b128 v[228:231], v207 offset:35840
	ds_read_b128 v[236:239], v207 offset:37888
	ds_read_b128 v[244:247], v207 offset:39936
	s_lshl_b64 s[2:3], s[38:39], 18
	s_add_u32 s4, s2, 0x40000
	s_addc_u32 s5, s3, 0
	s_add_u32 s2, s67, s4
	s_addc_u32 s3, s66, s5
	s_add_u32 s4, s35, s4
	s_addc_u32 s5, s34, s5
	s_add_i32 s94, s17, 2
	s_ashr_i32 s95, s94, 31
	s_lshl_b64 s[94:95], s[94:95], 7
	s_add_u32 s94, s8, s94
	s_addc_u32 s95, s9, s95
	s_add_u32 s94, s94, 0x80
	s_addc_u32 s95, s95, 0
	v_lshl_add_u64 v[250:251], s[94:95], 0, v[178:179]
	v_lshl_add_u64 v[252:253], s[94:95], 0, v[180:181]
	v_lshl_add_u64 v[222:223], s[94:95], 0, v[182:183]
	s_setprio 1
	s_waitcnt lgkmcnt(11)
	v_mfma_f32_16x16x32_bf16 v[158:161], v[162:165], v[214:217], v[158:161]
	v_mfma_f32_16x16x32_bf16 v[154:157], v[170:173], v[214:217], v[154:157]
	s_waitcnt lgkmcnt(10)
	v_mfma_f32_16x16x32_bf16 v[146:149], v[162:165], v[224:227], v[146:149]
	v_mfma_f32_16x16x32_bf16 v[138:141], v[170:173], v[224:227], v[138:141]
	s_waitcnt lgkmcnt(9)
	v_mfma_f32_16x16x32_bf16 v[130:133], v[162:165], v[232:235], v[130:133]
	v_mfma_f32_16x16x32_bf16 v[122:125], v[170:173], v[232:235], v[122:125]
	s_waitcnt lgkmcnt(8)
	v_mfma_f32_16x16x32_bf16 v[114:117], v[162:165], v[240:243], v[114:117]
	v_mfma_f32_16x16x32_bf16 v[106:109], v[170:173], v[240:243], v[106:109]
	ds_read_b64_tr_b16 v[162:163], v190 offset:49152
	ds_read_b64_tr_b16 v[164:165], v191 offset:49152
	ds_read_b64_tr_b16 v[170:171], v192 offset:49152
	ds_read_b64_tr_b16 v[172:173], v193 offset:49152
	s_waitcnt lgkmcnt(7)
	v_mfma_f32_16x16x32_bf16 v[158:161], v[166:169], v[218:221], v[158:161]
	v_mfma_f32_16x16x32_bf16 v[154:157], v[174:177], v[218:221], v[154:157]
	s_waitcnt lgkmcnt(6)
	v_mfma_f32_16x16x32_bf16 v[146:149], v[166:169], v[228:231], v[146:149]
	v_mfma_f32_16x16x32_bf16 v[138:141], v[174:177], v[228:231], v[138:141]
	s_waitcnt lgkmcnt(5)
	v_mfma_f32_16x16x32_bf16 v[130:133], v[166:169], v[236:239], v[130:133]
	v_mfma_f32_16x16x32_bf16 v[122:125], v[174:177], v[236:239], v[122:125]
	s_waitcnt lgkmcnt(4)
	v_mfma_f32_16x16x32_bf16 v[114:117], v[166:169], v[244:247], v[114:117]
	v_mfma_f32_16x16x32_bf16 v[106:109], v[174:177], v[244:247], v[106:109]
	ds_read_b64_tr_b16 v[166:167], v190 offset:57344
	ds_read_b64_tr_b16 v[168:169], v191 offset:57344
	ds_read_b64_tr_b16 v[174:175], v192 offset:57344
	ds_read_b64_tr_b16 v[176:177], v193 offset:57344
	s_waitcnt lgkmcnt(4)
	v_mfma_f32_16x16x32_bf16 v[150:153], v[162:165], v[214:217], v[150:153]
	v_mfma_f32_16x16x32_bf16 v[142:145], v[170:173], v[214:217], v[142:145]
	ds_read_b128 v[214:217], v207 offset:49152
	v_mfma_f32_16x16x32_bf16 v[134:137], v[162:165], v[224:227], v[134:137]
	v_mfma_f32_16x16x32_bf16 v[126:129], v[170:173], v[224:227], v[126:129]
	ds_read_b128 v[224:227], v207 offset:51200
	v_mfma_f32_16x16x32_bf16 v[118:121], v[162:165], v[232:235], v[118:121]
	v_mfma_f32_16x16x32_bf16 v[110:113], v[170:173], v[232:235], v[110:113]
	ds_read_b128 v[232:235], v207 offset:53248
	v_mfma_f32_16x16x32_bf16 v[102:105], v[162:165], v[240:243], v[102:105]
	v_mfma_f32_16x16x32_bf16 v[98:101], v[170:173], v[240:243], v[98:101]
	ds_read_b128 v[240:243], v207 offset:55296
	ds_read_b64_tr_b16 v[162:163], v190 offset:32768
	ds_read_b64_tr_b16 v[164:165], v191 offset:32768
	ds_read_b64_tr_b16 v[170:171], v192 offset:32768
	ds_read_b64_tr_b16 v[172:173], v193 offset:32768
	s_waitcnt lgkmcnt(8)
	v_mfma_f32_16x16x32_bf16 v[150:153], v[166:169], v[218:221], v[150:153]
	v_mfma_f32_16x16x32_bf16 v[142:145], v[174:177], v[218:221], v[142:145]
	ds_read_b128 v[218:221], v207 offset:50176
	v_mfma_f32_16x16x32_bf16 v[134:137], v[166:169], v[228:231], v[134:137]
	v_mfma_f32_16x16x32_bf16 v[126:129], v[174:177], v[228:231], v[126:129]
	ds_read_b128 v[228:231], v207 offset:52224
	v_mfma_f32_16x16x32_bf16 v[118:121], v[166:169], v[236:239], v[118:121]
	v_mfma_f32_16x16x32_bf16 v[110:113], v[174:177], v[236:239], v[110:113]
	ds_read_b128 v[236:239], v207 offset:54272
	v_mfma_f32_16x16x32_bf16 v[102:105], v[166:169], v[244:247], v[102:105]
	v_mfma_f32_16x16x32_bf16 v[98:101], v[174:177], v[244:247], v[98:101]
	ds_read_b128 v[244:247], v207 offset:56320
	ds_read_b64_tr_b16 v[166:167], v190 offset:40960
	ds_read_b64_tr_b16 v[168:169], v191 offset:40960
	ds_read_b64_tr_b16 v[174:175], v192 offset:40960
	ds_read_b64_tr_b16 v[176:177], v193 offset:40960
	s_waitcnt lgkmcnt(8)
	v_mfma_f32_16x16x32_bf16 v[94:97], v[162:165], v[214:217], v[94:97]
	v_mfma_f32_16x16x32_bf16 v[86:89], v[170:173], v[214:217], v[86:89]
	v_mfma_f32_16x16x32_bf16 v[78:81], v[162:165], v[224:227], v[78:81]
	v_mfma_f32_16x16x32_bf16 v[70:73], v[170:173], v[224:227], v[70:73]
	v_mfma_f32_16x16x32_bf16 v[62:65], v[162:165], v[232:235], v[62:65]
	v_mfma_f32_16x16x32_bf16 v[54:57], v[170:173], v[232:235], v[54:57]
	v_mfma_f32_16x16x32_bf16 v[46:49], v[162:165], v[240:243], v[46:49]
	v_mfma_f32_16x16x32_bf16 v[38:41], v[170:173], v[240:243], v[38:41]
	ds_read_b64_tr_b16 v[162:163], v190 offset:49152
	ds_read_b64_tr_b16 v[164:165], v191 offset:49152
	ds_read_b64_tr_b16 v[170:171], v192 offset:49152
	ds_read_b64_tr_b16 v[172:173], v193 offset:49152
	s_waitcnt lgkmcnt(4)
	v_mfma_f32_16x16x32_bf16 v[94:97], v[166:169], v[218:221], v[94:97]
	v_mfma_f32_16x16x32_bf16 v[86:89], v[174:177], v[218:221], v[86:89]
	v_mfma_f32_16x16x32_bf16 v[78:81], v[166:169], v[228:231], v[78:81]
	v_mfma_f32_16x16x32_bf16 v[70:73], v[174:177], v[228:231], v[70:73]
	v_mfma_f32_16x16x32_bf16 v[62:65], v[166:169], v[236:239], v[62:65]
	v_mfma_f32_16x16x32_bf16 v[54:57], v[174:177], v[236:239], v[54:57]
	v_mfma_f32_16x16x32_bf16 v[46:49], v[166:169], v[244:247], v[46:49]
	v_mfma_f32_16x16x32_bf16 v[38:41], v[174:177], v[244:247], v[38:41]
	ds_read_b64_tr_b16 v[166:167], v190 offset:57344
	ds_read_b64_tr_b16 v[168:169], v191 offset:57344
	ds_read_b64_tr_b16 v[174:175], v192 offset:57344
	ds_read_b64_tr_b16 v[176:177], v193 offset:57344
	s_waitcnt lgkmcnt(4)
	v_mfma_f32_16x16x32_bf16 v[90:93], v[162:165], v[214:217], v[90:93]
	v_mfma_f32_16x16x32_bf16 v[82:85], v[170:173], v[214:217], v[82:85]
	s_waitcnt vmcnt(9)
	v_cvt_pk_bf16_f32 v248, v2, v3
	v_cvt_pk_bf16_f32 v249, v4, v5
	ds_write_b64 v197, v[248:249] offset:16384
	global_load_dwordx4 v[2:5], v189, s[2:3]
	v_mfma_f32_16x16x32_bf16 v[74:77], v[162:165], v[224:227], v[74:77]
	v_mfma_f32_16x16x32_bf16 v[66:69], v[170:173], v[224:227], v[66:69]
	s_waitcnt vmcnt(9)
	v_cvt_pk_bf16_f32 v248, v6, v7
	v_cvt_pk_bf16_f32 v249, v8, v9
	ds_write_b64 v196, v[248:249] offset:16384
	global_load_dwordx4 v[6:9], v189, s[4:5]
	v_mfma_f32_16x16x32_bf16 v[58:61], v[162:165], v[232:235], v[58:61]
	v_mfma_f32_16x16x32_bf16 v[50:53], v[170:173], v[232:235], v[50:53]
	s_waitcnt vmcnt(9)
	v_cvt_pk_bf16_f32 v248, v10, v11
	v_cvt_pk_bf16_f32 v249, v12, v13
	ds_write_b64 v197, v[248:249]
	s_add_u32 s98, s2, 0x2000
	s_addc_u32 s99, s3, 0
	global_load_dwordx4 v[10:13], v189, s[98:99]
	v_mfma_f32_16x16x32_bf16 v[42:45], v[162:165], v[240:243], v[42:45]
	v_mfma_f32_16x16x32_bf16 v[30:33], v[170:173], v[240:243], v[30:33]
	s_waitcnt vmcnt(9)
	v_cvt_pk_bf16_f32 v248, v14, v15
	v_cvt_pk_bf16_f32 v249, v16, v17
	ds_write_b64 v195, v[248:249] offset:16384
	s_add_u32 s100, s4, 0x2000
	s_addc_u32 s101, s5, 0
	global_load_dwordx4 v[14:17], v189, s[100:101]
	s_waitcnt lgkmcnt(4)
	v_mfma_f32_16x16x32_bf16 v[90:93], v[166:169], v[218:221], v[90:93]
	v_mfma_f32_16x16x32_bf16 v[82:85], v[174:177], v[218:221], v[82:85]
	s_waitcnt vmcnt(9)
	v_cvt_pk_bf16_f32 v248, v18, v19
	v_cvt_pk_bf16_f32 v249, v20, v21
	ds_write_b64 v196, v[248:249]
	s_add_u32 s98, s2, 0x4000
	s_addc_u32 s99, s3, 0
	global_load_dwordx4 v[18:21], v189, s[98:99]
	v_mfma_f32_16x16x32_bf16 v[74:77], v[166:169], v[228:231], v[74:77]
	v_mfma_f32_16x16x32_bf16 v[66:69], v[174:177], v[228:231], v[66:69]
	s_waitcnt vmcnt(9)
	v_cvt_pk_bf16_f32 v248, v22, v23
	v_cvt_pk_bf16_f32 v249, v24, v25
	ds_write_b64 v194, v[248:249] offset:16384
	s_add_u32 s100, s4, 0x4000
	s_addc_u32 s101, s5, 0
	global_load_dwordx4 v[22:25], v189, s[100:101]
	v_mfma_f32_16x16x32_bf16 v[58:61], v[166:169], v[236:239], v[58:61]
	v_mfma_f32_16x16x32_bf16 v[50:53], v[174:177], v[236:239], v[50:53]
	s_waitcnt vmcnt(9)
	v_cvt_pk_bf16_f32 v248, v26, v27
	v_cvt_pk_bf16_f32 v249, v28, v29
	ds_write_b64 v195, v[248:249]
	s_add_u32 s98, s2, 0x6000
	s_addc_u32 s99, s3, 0
	global_load_dwordx4 v[26:29], v189, s[98:99]
	v_mfma_f32_16x16x32_bf16 v[42:45], v[166:169], v[244:247], v[42:45]
	v_mfma_f32_16x16x32_bf16 v[30:33], v[174:177], v[244:247], v[30:33]
	s_waitcnt vmcnt(9)
	v_cvt_pk_bf16_f32 v248, v34, v35
	v_cvt_pk_bf16_f32 v249, v36, v37
	ds_write_b64 v194, v[248:249]
	s_add_u32 s100, s4, 0x6000
	s_addc_u32 s101, s5, 0
	global_load_dwordx4 v[34:37], v189, s[100:101]
	v_lshl_add_u64 v[248:249], s[94:95], 0, v[184:185]
	s_setprio 0

.Lswp_guO_half:
	ds_read_b64_tr_b16 v[162:163], v190 offset:32768
	ds_read_b64_tr_b16 v[164:165], v191 offset:32768
	ds_read_b64_tr_b16 v[170:171], v192 offset:32768
	ds_read_b64_tr_b16 v[172:173], v193 offset:32768
	ds_read_b128 v[214:217], v207 offset:32768
	ds_read_b128 v[224:227], v207 offset:34816
	ds_read_b128 v[232:235], v207 offset:36864
	ds_read_b128 v[240:243], v207 offset:38912
	ds_read_b64_tr_b16 v[166:167], v190 offset:40960
	ds_read_b64_tr_b16 v[168:169], v191 offset:40960
	ds_read_b64_tr_b16 v[174:175], v192 offset:40960
	ds_read_b64_tr_b16 v[176:177], v193 offset:40960
	ds_read_b128 v[218:221], v207 offset:33792
	ds_read_b128 v[228:231], v207 offset:35840
	ds_read_b128 v[236:239], v207 offset:37888
	ds_read_b128 v[244:247], v207 offset:39936
	s_lshl_b64 s[2:3], s[38:39], 18
	s_add_u32 s4, s2, 0x40000
	s_addc_u32 s5, s3, 0
	s_add_u32 s2, s67, s4
	s_addc_u32 s3, s66, s5
	s_add_u32 s4, s35, s4
	s_addc_u32 s5, s34, s5
	s_add_i32 s94, s17, 2
	s_ashr_i32 s95, s94, 31
	s_lshl_b64 s[94:95], s[94:95], 7
	s_add_u32 s94, s8, s94
	s_addc_u32 s95, s9, s95
	s_add_u32 s94, s94, 0x80
	s_addc_u32 s95, s95, 0
	v_lshl_add_u64 v[250:251], s[94:95], 0, v[178:179]
	v_lshl_add_u64 v[252:253], s[94:95], 0, v[180:181]
	v_lshl_add_u64 v[222:223], s[94:95], 0, v[182:183]
	s_setprio 1
	s_waitcnt lgkmcnt(11)
	v_mfma_f32_16x16x32_bf16 v[158:161], v[162:165], v[214:217], v[158:161]
	v_mfma_f32_16x16x32_bf16 v[154:157], v[170:173], v[214:217], v[154:157]
	s_waitcnt lgkmcnt(10)
	v_mfma_f32_16x16x32_bf16 v[146:149], v[162:165], v[224:227], v[146:149]
	v_mfma_f32_16x16x32_bf16 v[138:141], v[170:173], v[224:227], v[138:141]
	s_waitcnt lgkmcnt(9)
	v_mfma_f32_16x16x32_bf16 v[130:133], v[162:165], v[232:235], v[130:133]
	v_mfma_f32_16x16x32_bf16 v[122:125], v[170:173], v[232:235], v[122:125]
	s_waitcnt lgkmcnt(8)
	v_mfma_f32_16x16x32_bf16 v[114:117], v[162:165], v[240:243], v[114:117]
	v_mfma_f32_16x16x32_bf16 v[106:109], v[170:173], v[240:243], v[106:109]
	ds_read_b64_tr_b16 v[162:163], v190 offset:49152
	ds_read_b64_tr_b16 v[164:165], v191 offset:49152
	ds_read_b64_tr_b16 v[170:171], v192 offset:49152
	ds_read_b64_tr_b16 v[172:173], v193 offset:49152
	s_waitcnt lgkmcnt(7)
	v_mfma_f32_16x16x32_bf16 v[158:161], v[166:169], v[218:221], v[158:161]
	v_mfma_f32_16x16x32_bf16 v[154:157], v[174:177], v[218:221], v[154:157]
	s_waitcnt lgkmcnt(6)
	v_mfma_f32_16x16x32_bf16 v[146:149], v[166:169], v[228:231], v[146:149]
	v_mfma_f32_16x16x32_bf16 v[138:141], v[174:177], v[228:231], v[138:141]
	s_waitcnt lgkmcnt(5)
	v_mfma_f32_16x16x32_bf16 v[130:133], v[166:169], v[236:239], v[130:133]
	v_mfma_f32_16x16x32_bf16 v[122:125], v[174:177], v[236:239], v[122:125]
	s_waitcnt lgkmcnt(4)
	v_mfma_f32_16x16x32_bf16 v[114:117], v[166:169], v[244:247], v[114:117]
	v_mfma_f32_16x16x32_bf16 v[106:109], v[174:177], v[244:247], v[106:109]
	ds_read_b64_tr_b16 v[166:167], v190 offset:57344
	ds_read_b64_tr_b16 v[168:169], v191 offset:57344
	ds_read_b64_tr_b16 v[174:175], v192 offset:57344
	ds_read_b64_tr_b16 v[176:177], v193 offset:57344
	s_waitcnt lgkmcnt(4)
	v_mfma_f32_16x16x32_bf16 v[150:153], v[162:165], v[214:217], v[150:153]
	v_mfma_f32_16x16x32_bf16 v[142:145], v[170:173], v[214:217], v[142:145]
	s_waitcnt vmcnt(9)
	v_cvt_pk_bf16_f32 v248, v2, v3
	v_cvt_pk_bf16_f32 v249, v4, v5
	ds_write_b64 v197, v[248:249] offset:16384
	global_load_dwordx4 v[2:5], v189, s[2:3]
	v_mfma_f32_16x16x32_bf16 v[134:137], v[162:165], v[224:227], v[134:137]
	v_mfma_f32_16x16x32_bf16 v[126:129], v[170:173], v[224:227], v[126:129]
	s_waitcnt vmcnt(9)
	v_cvt_pk_bf16_f32 v248, v6, v7
	v_cvt_pk_bf16_f32 v249, v8, v9
	ds_write_b64 v196, v[248:249] offset:16384
	global_load_dwordx4 v[6:9], v189, s[4:5]
	v_mfma_f32_16x16x32_bf16 v[118:121], v[162:165], v[232:235], v[118:121]
	v_mfma_f32_16x16x32_bf16 v[110:113], v[170:173], v[232:235], v[110:113]
	s_waitcnt vmcnt(9)
	v_cvt_pk_bf16_f32 v248, v10, v11
	v_cvt_pk_bf16_f32 v249, v12, v13
	ds_write_b64 v197, v[248:249]
	s_add_u32 s98, s2, 0x2000
	s_addc_u32 s99, s3, 0
	global_load_dwordx4 v[10:13], v189, s[98:99]
	v_mfma_f32_16x16x32_bf16 v[102:105], v[162:165], v[240:243], v[102:105]
	v_mfma_f32_16x16x32_bf16 v[98:101], v[170:173], v[240:243], v[98:101]
	s_waitcnt vmcnt(9)
	v_cvt_pk_bf16_f32 v248, v14, v15
	v_cvt_pk_bf16_f32 v249, v16, v17
	ds_write_b64 v195, v[248:249] offset:16384
	s_add_u32 s100, s4, 0x2000
	s_addc_u32 s101, s5, 0
	global_load_dwordx4 v[14:17], v189, s[100:101]
	s_waitcnt lgkmcnt(4)
	v_mfma_f32_16x16x32_bf16 v[150:153], v[166:169], v[218:221], v[150:153]
	v_mfma_f32_16x16x32_bf16 v[142:145], v[174:177], v[218:221], v[142:145]
	s_waitcnt vmcnt(9)
	v_cvt_pk_bf16_f32 v248, v18, v19
	v_cvt_pk_bf16_f32 v249, v20, v21
	ds_write_b64 v196, v[248:249]
	s_add_u32 s98, s2, 0x4000
	s_addc_u32 s99, s3, 0
	global_load_dwordx4 v[18:21], v189, s[98:99]
	v_mfma_f32_16x16x32_bf16 v[134:137], v[166:169], v[228:231], v[134:137]
	v_mfma_f32_16x16x32_bf16 v[126:129], v[174:177], v[228:231], v[126:129]
	s_waitcnt vmcnt(9)
	v_cvt_pk_bf16_f32 v248, v22, v23
	v_cvt_pk_bf16_f32 v249, v24, v25
	ds_write_b64 v194, v[248:249] offset:16384
	s_add_u32 s100, s4, 0x4000
	s_addc_u32 s101, s5, 0
	global_load_dwordx4 v[22:25], v189, s[100:101]
	v_mfma_f32_16x16x32_bf16 v[118:121], v[166:169], v[236:239], v[118:121]
	v_mfma_f32_16x16x32_bf16 v[110:113], v[174:177], v[236:239], v[110:113]
	s_waitcnt vmcnt(9)
	v_cvt_pk_bf16_f32 v248, v26, v27
	v_cvt_pk_bf16_f32 v249, v28, v29
	ds_write_b64 v195, v[248:249]
	s_add_u32 s98, s2, 0x6000
	s_addc_u32 s99, s3, 0
	global_load_dwordx4 v[26:29], v189, s[98:99]
	v_mfma_f32_16x16x32_bf16 v[102:105], v[166:169], v[244:247], v[102:105]
	v_mfma_f32_16x16x32_bf16 v[98:101], v[174:177], v[244:247], v[98:101]
	s_waitcnt vmcnt(9)
	v_cvt_pk_bf16_f32 v248, v34, v35
	v_cvt_pk_bf16_f32 v249, v36, v37
	ds_write_b64 v194, v[248:249]
	s_add_u32 s100, s4, 0x6000
	s_addc_u32 s101, s5, 0
	global_load_dwordx4 v[34:37], v189, s[100:101]
	v_lshl_add_u64 v[248:249], s[94:95], 0, v[184:185]
	s_setprio 0
	s_branch .Lswp_guO_tail

.LBB0_864:
	s_cmp_lg_u64 s[2:3], 0
	s_cbranch_scc1 .Lswp_dnO_half
	ds_read_b64_tr_b16 v[164:165], v190 offset:32768
	ds_read_b64_tr_b16 v[166:167], v191 offset:32768
	ds_read_b64_tr_b16 v[172:173], v192 offset:32768
	ds_read_b64_tr_b16 v[174:175], v193 offset:32768
	ds_read_b128 v[210:213], v207 offset:32768
	ds_read_b128 v[218:221], v207 offset:34816
	ds_read_b128 v[228:231], v207 offset:36864
	ds_read_b128 v[236:239], v207 offset:38912
	ds_read_b64_tr_b16 v[168:169], v190 offset:40960
	ds_read_b64_tr_b16 v[170:171], v191 offset:40960
	ds_read_b64_tr_b16 v[176:177], v192 offset:40960
	ds_read_b64_tr_b16 v[178:179], v193 offset:40960
	ds_read_b128 v[214:217], v207 offset:33792
	ds_read_b128 v[224:227], v207 offset:35840
	ds_read_b128 v[232:235], v207 offset:37888
	ds_read_b128 v[240:243], v207 offset:39936
	s_lshl_b64 s[2:3], s[48:49], 19
	s_add_u32 s48, s2, 0x80000
	s_addc_u32 s49, s3, 0
	s_add_u32 s2, s74, s48
	s_addc_u32 s3, s43, s49
	s_add_u32 s48, s37, s48
	s_addc_u32 s49, s35, s49
	s_add_i32 s94, s34, 2
	s_ashr_i32 s95, s94, 31
	s_lshl_b64 s[94:95], s[94:95], 7
	s_add_u32 s94, s22, s94
	s_addc_u32 s95, s23, s95
	s_add_u32 s94, s94, 0x80
	s_addc_u32 s95, s95, 0
	v_lshl_add_u64 v[250:251], s[94:95], 0, v[180:181]
	v_lshl_add_u64 v[252:253], s[94:95], 0, v[182:183]
	v_lshl_add_u64 v[222:223], s[94:95], 0, v[184:185]
	v_lshl_add_u64 v[246:247], s[94:95], 0, v[186:187]
	s_setprio 1
	s_waitcnt lgkmcnt(11)
	v_mfma_f32_16x16x32_bf16 v[160:163], v[164:167], v[210:213], v[160:163]
	v_mfma_f32_16x16x32_bf16 v[156:159], v[172:175], v[210:213], v[156:159]
	s_waitcnt lgkmcnt(10)
	v_mfma_f32_16x16x32_bf16 v[152:155], v[164:167], v[218:221], v[152:155]
	v_mfma_f32_16x16x32_bf16 v[148:151], v[172:175], v[218:221], v[148:151]
	s_waitcnt lgkmcnt(9)
	v_mfma_f32_16x16x32_bf16 v[136:139], v[164:167], v[228:231], v[136:139]
	v_mfma_f32_16x16x32_bf16 v[132:135], v[172:175], v[228:231], v[132:135]
	s_waitcnt lgkmcnt(8)
	v_mfma_f32_16x16x32_bf16 v[120:123], v[164:167], v[236:239], v[120:123]
	v_mfma_f32_16x16x32_bf16 v[116:119], v[172:175], v[236:239], v[116:119]
	ds_read_b64_tr_b16 v[164:165], v190 offset:49152
	ds_read_b64_tr_b16 v[166:167], v191 offset:49152
	ds_read_b64_tr_b16 v[172:173], v192 offset:49152
	ds_read_b64_tr_b16 v[174:175], v193 offset:49152
	s_waitcnt lgkmcnt(7)
	v_mfma_f32_16x16x32_bf16 v[160:163], v[168:171], v[214:217], v[160:163]
	v_mfma_f32_16x16x32_bf16 v[156:159], v[176:179], v[214:217], v[156:159]
	s_waitcnt lgkmcnt(6)
	v_mfma_f32_16x16x32_bf16 v[152:155], v[168:171], v[224:227], v[152:155]
	v_mfma_f32_16x16x32_bf16 v[148:151], v[176:179], v[224:227], v[148:151]
	s_waitcnt lgkmcnt(5)
	v_mfma_f32_16x16x32_bf16 v[136:139], v[168:171], v[232:235], v[136:139]
	v_mfma_f32_16x16x32_bf16 v[132:135], v[176:179], v[232:235], v[132:135]
	s_waitcnt lgkmcnt(4)
	v_mfma_f32_16x16x32_bf16 v[120:123], v[168:171], v[240:243], v[120:123]
	v_mfma_f32_16x16x32_bf16 v[116:119], v[176:179], v[240:243], v[116:119]
	ds_read_b64_tr_b16 v[168:169], v190 offset:57344
	ds_read_b64_tr_b16 v[170:171], v191 offset:57344
	ds_read_b64_tr_b16 v[176:177], v192 offset:57344
	ds_read_b64_tr_b16 v[178:179], v193 offset:57344
	s_waitcnt lgkmcnt(4)
	v_mfma_f32_16x16x32_bf16 v[144:147], v[164:167], v[210:213], v[144:147]
	v_mfma_f32_16x16x32_bf16 v[140:143], v[172:175], v[210:213], v[140:143]
	ds_read_b128 v[210:213], v207 offset:49152
	v_mfma_f32_16x16x32_bf16 v[128:131], v[164:167], v[218:221], v[128:131]
	v_mfma_f32_16x16x32_bf16 v[124:127], v[172:175], v[218:221], v[124:127]
	ds_read_b128 v[218:221], v207 offset:51200
	v_mfma_f32_16x16x32_bf16 v[112:115], v[164:167], v[228:231], v[112:115]
	v_mfma_f32_16x16x32_bf16 v[108:111], v[172:175], v[228:231], v[108:111]
	ds_read_b128 v[228:231], v207 offset:53248
	v_mfma_f32_16x16x32_bf16 v[104:107], v[164:167], v[236:239], v[104:107]
	v_mfma_f32_16x16x32_bf16 v[100:103], v[172:175], v[236:239], v[100:103]
	ds_read_b128 v[236:239], v207 offset:55296
	ds_read_b64_tr_b16 v[164:165], v190 offset:32768
	ds_read_b64_tr_b16 v[166:167], v191 offset:32768
	ds_read_b64_tr_b16 v[172:173], v192 offset:32768
	ds_read_b64_tr_b16 v[174:175], v193 offset:32768
	s_waitcnt lgkmcnt(8)
	v_mfma_f32_16x16x32_bf16 v[144:147], v[168:171], v[214:217], v[144:147]
	v_mfma_f32_16x16x32_bf16 v[140:143], v[176:179], v[214:217], v[140:143]
	ds_read_b128 v[214:217], v207 offset:50176
	v_mfma_f32_16x16x32_bf16 v[128:131], v[168:171], v[224:227], v[128:131]
	v_mfma_f32_16x16x32_bf16 v[124:127], v[176:179], v[224:227], v[124:127]
	ds_read_b128 v[224:227], v207 offset:52224
	v_mfma_f32_16x16x32_bf16 v[112:115], v[168:171], v[232:235], v[112:115]
	v_mfma_f32_16x16x32_bf16 v[108:111], v[176:179], v[232:235], v[108:111]
	ds_read_b128 v[232:235], v207 offset:54272
	v_mfma_f32_16x16x32_bf16 v[104:107], v[168:171], v[240:243], v[104:107]
	v_mfma_f32_16x16x32_bf16 v[100:103], v[176:179], v[240:243], v[100:103]
	ds_read_b128 v[240:243], v207 offset:56320
	ds_read_b64_tr_b16 v[168:169], v190 offset:40960
	ds_read_b64_tr_b16 v[170:171], v191 offset:40960
	ds_read_b64_tr_b16 v[176:177], v192 offset:40960
	ds_read_b64_tr_b16 v[178:179], v193 offset:40960
	s_waitcnt lgkmcnt(8)
	v_mfma_f32_16x16x32_bf16 v[80:83], v[164:167], v[210:213], v[80:83]
	v_mfma_f32_16x16x32_bf16 v[68:71], v[172:175], v[210:213], v[68:71]
	v_mfma_f32_16x16x32_bf16 v[48:51], v[164:167], v[218:221], v[48:51]
	v_mfma_f32_16x16x32_bf16 v[44:47], v[172:175], v[218:221], v[44:47]
	v_mfma_f32_16x16x32_bf16 v[32:35], v[164:167], v[228:231], v[32:35]
	v_mfma_f32_16x16x32_bf16 v[28:31], v[172:175], v[228:231], v[28:31]
	v_mfma_f32_16x16x32_bf16 v[16:19], v[164:167], v[236:239], v[16:19]
	v_mfma_f32_16x16x32_bf16 v[12:15], v[172:175], v[236:239], v[12:15]
	ds_read_b64_tr_b16 v[164:165], v190 offset:49152
	ds_read_b64_tr_b16 v[166:167], v191 offset:49152
	ds_read_b64_tr_b16 v[172:173], v192 offset:49152
	ds_read_b64_tr_b16 v[174:175], v193 offset:49152
	s_waitcnt lgkmcnt(4)
	v_mfma_f32_16x16x32_bf16 v[80:83], v[168:171], v[214:217], v[80:83]
	v_mfma_f32_16x16x32_bf16 v[68:71], v[176:179], v[214:217], v[68:71]
	v_mfma_f32_16x16x32_bf16 v[48:51], v[168:171], v[224:227], v[48:51]
	v_mfma_f32_16x16x32_bf16 v[44:47], v[176:179], v[224:227], v[44:47]
	v_mfma_f32_16x16x32_bf16 v[32:35], v[168:171], v[232:235], v[32:35]
	v_mfma_f32_16x16x32_bf16 v[28:31], v[176:179], v[232:235], v[28:31]
	v_mfma_f32_16x16x32_bf16 v[16:19], v[168:171], v[240:243], v[16:19]
	v_mfma_f32_16x16x32_bf16 v[12:15], v[176:179], v[240:243], v[12:15]
	ds_read_b64_tr_b16 v[168:169], v190 offset:57344
	ds_read_b64_tr_b16 v[170:171], v191 offset:57344
	ds_read_b64_tr_b16 v[176:177], v192 offset:57344
	ds_read_b64_tr_b16 v[178:179], v193 offset:57344
	s_waitcnt lgkmcnt(4)
	v_mfma_f32_16x16x32_bf16 v[56:59], v[164:167], v[210:213], v[56:59]
	v_mfma_f32_16x16x32_bf16 v[52:55], v[172:175], v[210:213], v[52:55]
	s_waitcnt vmcnt(9)
	v_cvt_pk_bf16_f32 v244, v64, v65
	v_cvt_pk_bf16_f32 v245, v66, v67
	ds_write_b64 v196, v[244:245] offset:16384
	global_load_dwordx4 v[64:67], v189, s[2:3]
	v_mfma_f32_16x16x32_bf16 v[40:43], v[164:167], v[218:221], v[40:43]
	v_mfma_f32_16x16x32_bf16 v[36:39], v[172:175], v[218:221], v[36:39]
	s_waitcnt vmcnt(9)
	v_cvt_pk_bf16_f32 v244, v60, v61
	v_cvt_pk_bf16_f32 v245, v62, v63
	ds_write_b64 v197, v[244:245] offset:16384
	global_load_dwordx4 v[60:63], v189, s[48:49]
	v_mfma_f32_16x16x32_bf16 v[24:27], v[164:167], v[228:231], v[24:27]
	v_mfma_f32_16x16x32_bf16 v[20:23], v[172:175], v[228:231], v[20:23]
	s_waitcnt vmcnt(9)
	v_cvt_pk_bf16_f32 v244, v76, v77
	v_cvt_pk_bf16_f32 v245, v78, v79
	ds_write_b64 v195, v[244:245] offset:16384
	s_add_u32 s98, s2, 0x4000
	s_addc_u32 s99, s3, 0
	global_load_dwordx4 v[76:79], v189, s[98:99]
	v_mfma_f32_16x16x32_bf16 v[8:11], v[164:167], v[236:239], v[8:11]
	v_mfma_f32_16x16x32_bf16 v[2:5], v[172:175], v[236:239], v[4:7]
	s_waitcnt vmcnt(9)
	v_cvt_pk_bf16_f32 v244, v72, v73
	v_cvt_pk_bf16_f32 v245, v74, v75
	ds_write_b64 v197, v[244:245]
	s_add_u32 s100, s48, 0x4000
	s_addc_u32 s101, s49, 0
	global_load_dwordx4 v[72:75], v189, s[100:101]
	s_waitcnt lgkmcnt(4)
	v_mfma_f32_16x16x32_bf16 v[56:59], v[168:171], v[214:217], v[56:59]
	v_mfma_f32_16x16x32_bf16 v[52:55], v[176:179], v[214:217], v[52:55]
	s_waitcnt vmcnt(9)
	v_cvt_pk_bf16_f32 v244, v88, v89
	v_cvt_pk_bf16_f32 v245, v90, v91
	ds_write_b64 v194, v[244:245] offset:16384
	s_add_u32 s98, s2, 0x8000
	s_addc_u32 s99, s3, 0
	global_load_dwordx4 v[88:91], v189, s[98:99]
	v_mfma_f32_16x16x32_bf16 v[40:43], v[168:171], v[224:227], v[40:43]
	v_mfma_f32_16x16x32_bf16 v[36:39], v[176:179], v[224:227], v[36:39]
	s_waitcnt vmcnt(9)
	v_cvt_pk_bf16_f32 v244, v84, v85
	v_cvt_pk_bf16_f32 v245, v86, v87
	ds_write_b64 v196, v[244:245]
	s_add_u32 s100, s48, 0x8000
	s_addc_u32 s101, s49, 0
	global_load_dwordx4 v[84:87], v189, s[100:101]
	v_mfma_f32_16x16x32_bf16 v[24:27], v[168:171], v[232:235], v[24:27]
	v_mfma_f32_16x16x32_bf16 v[20:23], v[176:179], v[232:235], v[20:23]
	s_waitcnt vmcnt(9)
	v_cvt_pk_bf16_f32 v244, v96, v97
	v_cvt_pk_bf16_f32 v245, v98, v99
	ds_write_b64 v194, v[244:245]
	s_add_u32 s98, s2, 0xc000
	s_addc_u32 s99, s3, 0
	global_load_dwordx4 v[96:99], v189, s[98:99]
	v_mfma_f32_16x16x32_bf16 v[8:11], v[168:171], v[240:243], v[8:11]
	v_mfma_f32_16x16x32_bf16 v[4:7], v[176:179], v[240:243], v[2:5]
	s_waitcnt vmcnt(9)
	v_cvt_pk_bf16_f32 v244, v92, v93
	v_cvt_pk_bf16_f32 v245, v94, v95
	ds_write_b64 v195, v[244:245]
	s_add_u32 s100, s48, 0xc000
	s_addc_u32 s101, s49, 0
	global_load_dwordx4 v[92:95], v189, s[100:101]
	s_setprio 0

.Lswp_dnO_half:
	ds_read_b64_tr_b16 v[164:165], v190 offset:32768
	ds_read_b64_tr_b16 v[166:167], v191 offset:32768
	ds_read_b64_tr_b16 v[172:173], v192 offset:32768
	ds_read_b64_tr_b16 v[174:175], v193 offset:32768
	ds_read_b128 v[210:213], v207 offset:32768
	ds_read_b128 v[218:221], v207 offset:34816
	ds_read_b128 v[228:231], v207 offset:36864
	ds_read_b128 v[236:239], v207 offset:38912
	ds_read_b64_tr_b16 v[168:169], v190 offset:40960
	ds_read_b64_tr_b16 v[170:171], v191 offset:40960
	ds_read_b64_tr_b16 v[176:177], v192 offset:40960
	ds_read_b64_tr_b16 v[178:179], v193 offset:40960
	ds_read_b128 v[214:217], v207 offset:33792
	ds_read_b128 v[224:227], v207 offset:35840
	ds_read_b128 v[232:235], v207 offset:37888
	ds_read_b128 v[240:243], v207 offset:39936
	s_lshl_b64 s[2:3], s[48:49], 19
	s_add_u32 s48, s2, 0x80000
	s_addc_u32 s49, s3, 0
	s_add_u32 s2, s74, s48
	s_addc_u32 s3, s43, s49
	s_add_u32 s48, s37, s48
	s_addc_u32 s49, s35, s49
	s_add_i32 s94, s34, 2
	s_ashr_i32 s95, s94, 31
	s_lshl_b64 s[94:95], s[94:95], 7
	s_add_u32 s94, s22, s94
	s_addc_u32 s95, s23, s95
	s_add_u32 s94, s94, 0x80
	s_addc_u32 s95, s95, 0
	v_lshl_add_u64 v[250:251], s[94:95], 0, v[180:181]
	v_lshl_add_u64 v[252:253], s[94:95], 0, v[182:183]
	v_lshl_add_u64 v[222:223], s[94:95], 0, v[184:185]
	v_lshl_add_u64 v[246:247], s[94:95], 0, v[186:187]
	s_setprio 1
	s_waitcnt lgkmcnt(11)
	v_mfma_f32_16x16x32_bf16 v[160:163], v[164:167], v[210:213], v[160:163]
	v_mfma_f32_16x16x32_bf16 v[156:159], v[172:175], v[210:213], v[156:159]
	s_waitcnt lgkmcnt(10)
	v_mfma_f32_16x16x32_bf16 v[152:155], v[164:167], v[218:221], v[152:155]
	v_mfma_f32_16x16x32_bf16 v[148:151], v[172:175], v[218:221], v[148:151]
	s_waitcnt lgkmcnt(9)
	v_mfma_f32_16x16x32_bf16 v[136:139], v[164:167], v[228:231], v[136:139]
	v_mfma_f32_16x16x32_bf16 v[132:135], v[172:175], v[228:231], v[132:135]
	s_waitcnt lgkmcnt(8)
	v_mfma_f32_16x16x32_bf16 v[120:123], v[164:167], v[236:239], v[120:123]
	v_mfma_f32_16x16x32_bf16 v[116:119], v[172:175], v[236:239], v[116:119]
	ds_read_b64_tr_b16 v[164:165], v190 offset:49152
	ds_read_b64_tr_b16 v[166:167], v191 offset:49152
	ds_read_b64_tr_b16 v[172:173], v192 offset:49152
	ds_read_b64_tr_b16 v[174:175], v193 offset:49152
	s_waitcnt lgkmcnt(7)
	v_mfma_f32_16x16x32_bf16 v[160:163], v[168:171], v[214:217], v[160:163]
	v_mfma_f32_16x16x32_bf16 v[156:159], v[176:179], v[214:217], v[156:159]
	s_waitcnt lgkmcnt(6)
	v_mfma_f32_16x16x32_bf16 v[152:155], v[168:171], v[224:227], v[152:155]
	v_mfma_f32_16x16x32_bf16 v[148:151], v[176:179], v[224:227], v[148:151]
	s_waitcnt lgkmcnt(5)
	v_mfma_f32_16x16x32_bf16 v[136:139], v[168:171], v[232:235], v[136:139]
	v_mfma_f32_16x16x32_bf16 v[132:135], v[176:179], v[232:235], v[132:135]
	s_waitcnt lgkmcnt(4)
	v_mfma_f32_16x16x32_bf16 v[120:123], v[168:171], v[240:243], v[120:123]
	v_mfma_f32_16x16x32_bf16 v[116:119], v[176:179], v[240:243], v[116:119]
	ds_read_b64_tr_b16 v[168:169], v190 offset:57344
	ds_read_b64_tr_b16 v[170:171], v191 offset:57344
	ds_read_b64_tr_b16 v[176:177], v192 offset:57344
	ds_read_b64_tr_b16 v[178:179], v193 offset:57344
	s_waitcnt lgkmcnt(4)
	v_mfma_f32_16x16x32_bf16 v[144:147], v[164:167], v[210:213], v[144:147]
	v_mfma_f32_16x16x32_bf16 v[140:143], v[172:175], v[210:213], v[140:143]
	s_waitcnt vmcnt(9)
	v_cvt_pk_bf16_f32 v244, v64, v65
	v_cvt_pk_bf16_f32 v245, v66, v67
	ds_write_b64 v196, v[244:245] offset:16384
	global_load_dwordx4 v[64:67], v189, s[2:3]
	v_mfma_f32_16x16x32_bf16 v[128:131], v[164:167], v[218:221], v[128:131]
	v_mfma_f32_16x16x32_bf16 v[124:127], v[172:175], v[218:221], v[124:127]
	s_waitcnt vmcnt(9)
	v_cvt_pk_bf16_f32 v244, v60, v61
	v_cvt_pk_bf16_f32 v245, v62, v63
	ds_write_b64 v197, v[244:245] offset:16384
	global_load_dwordx4 v[60:63], v189, s[48:49]
	v_mfma_f32_16x16x32_bf16 v[112:115], v[164:167], v[228:231], v[112:115]
	v_mfma_f32_16x16x32_bf16 v[108:111], v[172:175], v[228:231], v[108:111]
	s_waitcnt vmcnt(9)
	v_cvt_pk_bf16_f32 v244, v76, v77
	v_cvt_pk_bf16_f32 v245, v78, v79
	ds_write_b64 v195, v[244:245] offset:16384
	s_add_u32 s98, s2, 0x4000
	s_addc_u32 s99, s3, 0
	global_load_dwordx4 v[76:79], v189, s[98:99]
	v_mfma_f32_16x16x32_bf16 v[104:107], v[164:167], v[236:239], v[104:107]
	v_mfma_f32_16x16x32_bf16 v[100:103], v[172:175], v[236:239], v[100:103]
	s_waitcnt vmcnt(9)
	v_cvt_pk_bf16_f32 v244, v72, v73
	v_cvt_pk_bf16_f32 v245, v74, v75
	ds_write_b64 v197, v[244:245]
	s_add_u32 s100, s48, 0x4000
	s_addc_u32 s101, s49, 0
	global_load_dwordx4 v[72:75], v189, s[100:101]
	s_waitcnt lgkmcnt(4)
	v_mfma_f32_16x16x32_bf16 v[144:147], v[168:171], v[214:217], v[144:147]
	v_mfma_f32_16x16x32_bf16 v[140:143], v[176:179], v[214:217], v[140:143]
	s_waitcnt vmcnt(9)
	v_cvt_pk_bf16_f32 v244, v88, v89
	v_cvt_pk_bf16_f32 v245, v90, v91
	ds_write_b64 v194, v[244:245] offset:16384
	s_add_u32 s98, s2, 0x8000
	s_addc_u32 s99, s3, 0
	global_load_dwordx4 v[88:91], v189, s[98:99]
	v_mfma_f32_16x16x32_bf16 v[128:131], v[168:171], v[224:227], v[128:131]
	v_mfma_f32_16x16x32_bf16 v[124:127], v[176:179], v[224:227], v[124:127]
	s_waitcnt vmcnt(9)
	v_cvt_pk_bf16_f32 v244, v84, v85
	v_cvt_pk_bf16_f32 v245, v86, v87
	ds_write_b64 v196, v[244:245]
	s_add_u32 s100, s48, 0x8000
	s_addc_u32 s101, s49, 0
	global_load_dwordx4 v[84:87], v189, s[100:101]
	v_mfma_f32_16x16x32_bf16 v[112:115], v[168:171], v[232:235], v[112:115]
	v_mfma_f32_16x16x32_bf16 v[108:111], v[176:179], v[232:235], v[108:111]
	s_waitcnt vmcnt(9)
	v_cvt_pk_bf16_f32 v244, v96, v97
	v_cvt_pk_bf16_f32 v245, v98, v99
	ds_write_b64 v194, v[244:245]
	s_add_u32 s98, s2, 0xc000
	s_addc_u32 s99, s3, 0
	global_load_dwordx4 v[96:99], v189, s[98:99]
	v_mfma_f32_16x16x32_bf16 v[104:107], v[168:171], v[240:243], v[104:107]
	v_mfma_f32_16x16x32_bf16 v[100:103], v[176:179], v[240:243], v[100:103]
	s_waitcnt vmcnt(9)
	v_cvt_pk_bf16_f32 v244, v92, v93
	v_cvt_pk_bf16_f32 v245, v94, v95
	ds_write_b64 v195, v[244:245]
	s_add_u32 s100, s48, 0xc000
	s_addc_u32 s101, s49, 0
	global_load_dwordx4 v[92:95], v189, s[100:101]
	s_setprio 0
	s_branch .Lswp_dnO_tail
